# C1 combine: the 12 next-layer norm/modulation loads per row also issued before the prefetch block into free registers (copied into place after one counted wait), so the next row's 12 loads stay in fli
# speedup vs baseline: 1.0038x; 1.0009x over previous
.LBB0_3036:
	s_add_i32 s10, s6, 0x800
	s_cmp_lt_i32 s10, s36
	s_cselect_b64 s[12:13], -1, 0
	s_and_b64 s[14:15], s[12:13], exec
	s_cselect_b32 s14, s10, s6
	s_ashr_i32 s15, s14, 31
	s_lshl_b64 s[16:17], s[14:15], 13
	v_lshl_add_u64 v[50:51], v[118:119], 0, s[16:17]
	s_movk_i32 s4, 0x1000
	v_add_co_u32_e32 v52, vcc, s4, v50
	s_min_i32 s4, s6, 0x4000
	s_lshl_b64 s[14:15], s[14:15], 12
	s_ashr_i32 s4, s4, 12
	s_waitcnt vmcnt(9)
	v_lshlrev_b32_e32 v100, 16, v2
	v_and_b32_e32 v101, 0xffff0000, v2
	v_lshlrev_b32_e32 v102, 16, v3
	v_and_b32_e32 v103, 0xffff0000, v3
	v_lshl_add_u64 v[54:55], v[120:121], 0, s[14:15]
	s_mul_hi_i32 s15, s4, 0x1800
	s_mul_i32 s14, s4, 0x1800
	v_pk_add_f32 v[102:103], v[102:103], 0 op_sel_hi:[1,0]
	v_pk_add_f32 v[100:101], v[100:101], 0 op_sel_hi:[1,0]
	v_lshlrev_b32_e32 v104, 16, v4
	v_and_b32_e32 v105, 0xffff0000, v4
	v_lshlrev_b32_e32 v106, 16, v5
	v_and_b32_e32 v107, 0xffff0000, v5
	s_waitcnt vmcnt(7)
	v_lshlrev_b32_e32 v108, 16, v14
	v_and_b32_e32 v109, 0xffff0000, v14
	v_lshlrev_b32_e32 v110, 16, v15
	v_and_b32_e32 v111, 0xffff0000, v15
	s_lshl_b64 s[14:15], s[14:15], 2
	v_pk_add_f32 v[106:107], v[106:107], 0 op_sel_hi:[1,0]
	v_pk_add_f32 v[104:105], v[104:105], 0 op_sel_hi:[1,0]
	v_pk_add_f32 v[100:101], v[100:101], v[108:109]
	v_pk_add_f32 v[102:103], v[102:103], v[110:111]
	v_lshlrev_b32_e32 v108, 16, v16
	v_and_b32_e32 v109, 0xffff0000, v16
	v_lshlrev_b32_e32 v110, 16, v17
	v_and_b32_e32 v111, 0xffff0000, v17
	s_add_u32 s4, s37, s14
	v_pk_add_f32 v[104:105], v[104:105], v[108:109]
	v_pk_add_f32 v[106:107], v[106:107], v[110:111]
	s_waitcnt vmcnt(5)
	v_lshlrev_b32_e32 v108, 16, v18
	v_and_b32_e32 v109, 0xffff0000, v18
	v_lshlrev_b32_e32 v110, 16, v19
	v_and_b32_e32 v111, 0xffff0000, v19
	s_addc_u32 s7, s38, s15
	v_pk_add_f32 v[102:103], v[102:103], v[110:111]
	v_pk_add_f32 v[100:101], v[100:101], v[108:109]
	v_lshlrev_b32_e32 v108, 16, v20
	v_and_b32_e32 v109, 0xffff0000, v20
	v_lshlrev_b32_e32 v110, 16, v21
	v_and_b32_e32 v111, 0xffff0000, v21
	s_add_u32 s16, s4, 0x5000
	v_pk_add_f32 v[106:107], v[106:107], v[110:111]
	v_pk_add_f32 v[104:105], v[104:105], v[108:109]
	s_waitcnt vmcnt(3)
	v_lshlrev_b32_e32 v108, 16, v26
	v_and_b32_e32 v109, 0xffff0000, v26
	v_lshlrev_b32_e32 v110, 16, v27
	v_and_b32_e32 v111, 0xffff0000, v27
	v_addc_co_u32_e32 v53, vcc, 0, v51, vcc
	s_addc_u32 s17, s7, 0
	v_pk_add_f32 v[100:101], v[100:101], v[108:109]
	v_pk_add_f32 v[112:113], v[102:103], v[110:111]
	v_lshlrev_b32_e32 v102, 16, v28
	v_and_b32_e32 v103, 0xffff0000, v28
	v_lshlrev_b32_e32 v108, 16, v29
	v_and_b32_e32 v109, 0xffff0000, v29
	v_lshlrev_b32_e32 v117, 2, v116
	v_lshlrev_b32_e32 v123, 2, v122
	v_pk_add_f32 v[114:115], v[104:105], v[102:103]
	v_pk_add_f32 v[130:131], v[106:107], v[108:109]
	global_load_dwordx4 v[108:111], v117, s[16:17] offset:16
	global_load_dwordx4 v[102:105], v117, s[16:17]
	global_load_dwordx4 v[154:157], v123, s[16:17] offset:16
	global_load_dwordx4 v[158:161], v123, s[16:17]
	s_add_u32 s14, s39, s14
	s_addc_u32 s15, s40, s15
	s_add_u32 s16, s14, 0x1000
	s_addc_u32 s17, s15, 0
	global_load_dwordx4 v[174:177], v[124:125], off offset:16
	global_load_dwordx4 v[178:181], v[124:125], off
	global_load_dwordx4 v[182:185], v117, s[16:17] offset:16
	global_load_dwordx4 v[186:189], v117, s[16:17]
	global_load_dwordx4 v[190:193], v117, s[14:15] offset:16
	global_load_dwordx4 v[194:197], v117, s[14:15]
	global_load_dwordx4 v[198:201], v[124:125], off offset:2064
	global_load_dwordx4 v[202:205], v[124:125], off offset:2048
	global_load_dwordx4 v[206:209], v123, s[16:17] offset:16
	global_load_dwordx4 v[210:213], v123, s[16:17]
	global_load_dwordx4 v[226:229], v117, s[14:15] offset:2064
	global_load_dwordx4 v[230:233], v117, s[14:15] offset:2048
	global_load_dwordx4 v[94:97], v[50:51], off nt
	global_load_dwordx4 v[90:93], v[50:51], off offset:2048 nt
	global_load_dwordx4 v[86:89], v[52:53], off nt
	global_load_dwordx4 v[82:85], v[52:53], off offset:2048 nt
	global_load_dwordx4 v[74:77], v[54:55], off offset:16
	global_load_dwordx4 v[78:81], v[54:55], off
	global_load_dwordx4 v[70:73], v[50:51], off offset:1024 nt
	global_load_dwordx4 v[66:69], v[50:51], off offset:3072 nt
	global_load_dwordx4 v[62:65], v[52:53], off offset:1024 nt
	global_load_dwordx4 v[58:61], v[52:53], off offset:3072 nt
	s_nop 0
	global_load_dwordx4 v[50:53], v[54:55], off offset:2064
	s_nop 0
	global_load_dwordx4 v[54:57], v[54:55], off offset:2048
	v_lshlrev_b32_e32 v132, 16, v30
	v_and_b32_e32 v133, 0xffff0000, v30
	v_lshlrev_b32_e32 v134, 16, v31
	v_and_b32_e32 v135, 0xffff0000, v31
	s_ashr_i32 s7, s6, 31
	s_lshl_b64 s[18:19], s[6:7], 12
	v_cndmask_b32_e64 v98, 0, 1, s[8:9]
	v_cmp_ne_u32_e64 s[34:35], 1, v98
	s_andn2_b64 vcc, exec, s[8:9]
	s_waitcnt vmcnt(26)
	v_pk_fma_f32 v[106:107], v[112:113], v[104:105], v[12:13]
	v_pk_fma_f32 v[104:105], v[100:101], v[102:103], v[10:11]
	v_pk_fma_f32 v[102:103], v[130:131], v[110:111], v[8:9]
	v_pk_fma_f32 v[100:101], v[114:115], v[108:109], v[6:7]
	v_lshlrev_b32_e32 v108, 16, v22
	v_and_b32_e32 v109, 0xffff0000, v22
	v_lshlrev_b32_e32 v110, 16, v23
	v_and_b32_e32 v111, 0xffff0000, v23
	v_pk_add_f32 v[110:111], v[110:111], 0 op_sel_hi:[1,0]
	v_pk_add_f32 v[108:109], v[108:109], 0 op_sel_hi:[1,0]
	v_lshlrev_b32_e32 v112, 16, v24
	v_and_b32_e32 v113, 0xffff0000, v24
	v_lshlrev_b32_e32 v114, 16, v25
	v_and_b32_e32 v115, 0xffff0000, v25
	v_pk_add_f32 v[114:115], v[114:115], 0 op_sel_hi:[1,0]
	v_pk_add_f32 v[112:113], v[112:113], 0 op_sel_hi:[1,0]
	v_pk_add_f32 v[108:109], v[108:109], v[132:133]
	v_pk_add_f32 v[110:111], v[110:111], v[134:135]
	v_lshlrev_b32_e32 v132, 16, v32
	v_and_b32_e32 v133, 0xffff0000, v32
	v_lshlrev_b32_e32 v134, 16, v33
	v_and_b32_e32 v135, 0xffff0000, v33
	v_pk_add_f32 v[112:113], v[112:113], v[132:133]
	v_pk_add_f32 v[114:115], v[114:115], v[134:135]
	v_lshlrev_b32_e32 v132, 16, v34
	v_and_b32_e32 v133, 0xffff0000, v34
	v_lshlrev_b32_e32 v134, 16, v35
	v_and_b32_e32 v135, 0xffff0000, v35
	v_pk_add_f32 v[110:111], v[110:111], v[134:135]
	v_pk_add_f32 v[108:109], v[108:109], v[132:133]
	v_lshlrev_b32_e32 v132, 16, v36
	v_and_b32_e32 v133, 0xffff0000, v36
	v_lshlrev_b32_e32 v134, 16, v37
	v_and_b32_e32 v135, 0xffff0000, v37
	v_lshl_add_u64 v[130:131], v[126:127], 0, s[18:19]
	v_pk_add_f32 v[114:115], v[114:115], v[134:135]
	v_pk_add_f32 v[112:113], v[112:113], v[132:133]
	v_lshlrev_b32_e32 v132, 16, v38
	v_and_b32_e32 v133, 0xffff0000, v38
	v_lshlrev_b32_e32 v134, 16, v39
	v_and_b32_e32 v135, 0xffff0000, v39
	global_store_dwordx4 v[130:131], v[104:107], off
	global_store_dwordx4 v[130:131], v[100:103], off offset:16
	v_pk_add_f32 v[132:133], v[108:109], v[132:133]
	v_pk_add_f32 v[134:135], v[110:111], v[134:135]
	v_lshlrev_b32_e32 v108, 16, v40
	v_and_b32_e32 v109, 0xffff0000, v40
	v_lshlrev_b32_e32 v110, 16, v41
	v_and_b32_e32 v111, 0xffff0000, v41
	v_pk_add_f32 v[136:137], v[112:113], v[108:109]
	v_pk_add_f32 v[138:139], v[114:115], v[110:111]
	s_waitcnt vmcnt(26)
	v_pk_fma_f32 v[110:111], v[138:139], v[156:157], v[44:45]
	v_pk_fma_f32 v[114:115], v[134:135], v[160:161], v[48:49]
	v_pk_fma_f32 v[112:113], v[132:133], v[158:159], v[46:47]
	v_pk_fma_f32 v[108:109], v[136:137], v[154:155], v[42:43]
	global_store_dwordx4 v[130:131], v[112:115], off offset:2048
	global_store_dwordx4 v[130:131], v[108:111], off offset:2064
	s_cbranch_vccnz .LBB0_3038
	v_pk_mul_f32 v[130:131], v[106:107], v[106:107]
	v_pk_mul_f32 v[132:133], v[104:105], v[104:105]
	v_mul_f32_e32 v98, v108, v108
	v_pk_mov_b32 v[134:135], v[132:133], v[130:131] op_sel:[1,0]
	v_mov_b32_e32 v133, v131
	v_pk_add_f32 v[130:131], v[134:135], v[132:133]
	v_pk_mul_f32 v[132:133], v[102:103], v[102:103]
	v_pk_mul_f32 v[134:135], v[100:101], v[100:101]
	v_pk_add_f32 v[130:131], v[130:131], v[130:131] op_sel:[0,1] op_sel_hi:[1,0]
	v_pk_mov_b32 v[136:137], v[134:135], v[132:133] op_sel:[1,0]
	v_mov_b32_e32 v135, v133
	v_pk_add_f32 v[132:133], v[136:137], v[134:135]
	v_mul_f32_e32 v134, v109, v109
	v_pk_add_f32 v[132:133], v[132:133], v[132:133] op_sel:[0,1] op_sel_hi:[1,0]
	v_mov_b32_e32 v131, v98
	v_mov_b32_e32 v133, v134
	v_mul_f32_e32 v98, v113, v113
	v_mul_f32_e32 v135, v110, v110
	v_pk_add_f32 v[130:131], v[130:131], v[132:133]
	v_pk_fma_f32 v[132:133], v[112:113], v[112:113], v[98:99] op_sel_hi:[1,1,0]
	v_mul_f32_e32 v98, v115, v115
	v_mul_f32_e32 v136, v111, v111
	v_mov_b32_e32 v133, v135
	v_pk_fma_f32 v[134:135], v[114:115], v[114:115], v[98:99] op_sel_hi:[1,1,0]
	v_mov_b32_e32 v135, v136
	v_pk_add_f32 v[132:133], v[132:133], v[134:135]
	v_pk_add_f32 v[130:131], v[130:131], v[132:133]
	v_add_f32_e32 v98, v130, v131
	v_and_b32_e32 v131, 64, v214
	v_xor_b32_e32 v130, 16, v214
	v_add_f32_dpp v98, v98, v98 quad_perm:[1,0,3,2] row_mask:0xf bank_mask:0xf bound_ctrl:1
	v_add_u32_e32 v131, 64, v131
	v_cmp_lt_i32_e32 vcc, v130, v131
	v_add_f32_dpp v98, v98, v98 quad_perm:[2,3,0,1] row_mask:0xf bank_mask:0xf bound_ctrl:1
	v_cndmask_b32_e32 v130, v214, v130, vcc
	v_add_f32_dpp v98, v98, v98 row_half_mirror row_mask:0xf bank_mask:0xf bound_ctrl:1
	v_lshlrev_b32_e32 v130, 2, v130
	s_lshl_b64 s[18:19], s[6:7], 11
	v_add_f32_dpp v98, v98, v98 row_mirror row_mask:0xf bank_mask:0xf bound_ctrl:1
	ds_bpermute_b32 v130, v130, v98
	s_waitcnt lgkmcnt(0)
	v_add_f32_e32 v98, v98, v130
	v_xor_b32_e32 v130, 32, v214
	v_cmp_lt_i32_e32 vcc, v130, v131
	s_nop 1
	v_cndmask_b32_e32 v130, v214, v130, vcc
	v_lshlrev_b32_e32 v130, 2, v130
	ds_bpermute_b32 v130, v130, v98
	s_waitcnt lgkmcnt(0)
	v_add_f32_e32 v98, v98, v130
	v_fmamk_f32 v98, v98, 0x3a800000, v1
	v_cmp_gt_f32_e32 vcc, s77, v98
	v_mul_f32_e32 v130, 0x4b800000, v98
	s_nop 0
	v_cndmask_b32_e32 v98, v98, v130, vcc
	v_rsq_f32_e32 v98, v98
	s_nop 0
	v_mul_f32_e32 v130, 0x45800000, v98
	v_cndmask_b32_e32 v98, v98, v130, vcc
	s_waitcnt vmcnt(22)
	v_mov_b64_e32 v[130:131], v[174:175]
	v_mov_b64_e32 v[132:133], v[176:177]
	v_mov_b64_e32 v[134:135], v[178:179]
	v_mov_b64_e32 v[136:137], v[180:181]
	v_mov_b64_e32 v[138:139], v[182:183]
	v_mov_b64_e32 v[140:141], v[184:185]
	v_mov_b64_e32 v[142:143], v[186:187]
	v_mov_b64_e32 v[144:145], v[188:189]
	v_mov_b64_e32 v[146:147], v[190:191]
	v_mov_b64_e32 v[148:149], v[192:193]
	v_mov_b64_e32 v[150:151], v[194:195]
	v_mov_b64_e32 v[152:153], v[196:197]
	v_pk_mul_f32 v[106:107], v[106:107], v[98:99] op_sel_hi:[1,0]
	v_pk_mul_f32 v[104:105], v[104:105], v[98:99] op_sel_hi:[1,0]
	v_pk_mul_f32 v[102:103], v[102:103], v[98:99] op_sel_hi:[1,0]
	v_pk_mul_f32 v[100:101], v[100:101], v[98:99] op_sel_hi:[1,0]
	v_pk_mul_f32 v[114:115], v[114:115], v[98:99] op_sel_hi:[1,0]
	v_pk_mul_f32 v[112:113], v[112:113], v[98:99] op_sel_hi:[1,0]
	v_pk_mul_f32 v[110:111], v[110:111], v[98:99] op_sel_hi:[1,0]
	v_pk_mul_f32 v[108:109], v[108:109], v[98:99] op_sel_hi:[1,0]
	v_pk_mul_f32 v[100:101], v[130:131], v[100:101]
	v_pk_mul_f32 v[104:105], v[134:135], v[104:105]
	v_pk_mul_f32 v[106:107], v[136:137], v[106:107]
	v_pk_add_f32 v[134:135], v[144:145], 1.0 op_sel_hi:[1,0]
	v_pk_add_f32 v[136:137], v[142:143], 1.0 op_sel_hi:[1,0]
	v_pk_mul_f32 v[102:103], v[132:133], v[102:103]
	v_pk_add_f32 v[130:131], v[140:141], 1.0 op_sel_hi:[1,0]
	v_pk_add_f32 v[132:133], v[138:139], 1.0 op_sel_hi:[1,0]
	v_pk_fma_f32 v[106:107], v[134:135], v[106:107], v[152:153]
	v_pk_fma_f32 v[104:105], v[136:137], v[104:105], v[150:151]
	v_pk_fma_f32 v[130:131], v[130:131], v[102:103], v[148:149]
	v_pk_fma_f32 v[102:103], v[132:133], v[100:101], v[146:147]
	v_cvt_pk_bf16_f32 v100, v104, v105
	v_cvt_pk_bf16_f32 v101, v106, v107
	v_cvt_pk_bf16_f32 v102, v102, v103
	v_cvt_pk_bf16_f32 v103, v130, v131
	v_lshl_add_u64 v[146:147], v[128:129], 0, s[18:19]
	global_store_dwordx4 v[146:147], v[100:103], off
	s_waitcnt vmcnt(17)
	s_nop 1
	v_mov_b64_e32 v[100:101], v[198:199]
	v_mov_b64_e32 v[102:103], v[200:201]
	s_nop 0
	v_mov_b64_e32 v[104:105], v[202:203]
	v_mov_b64_e32 v[106:107], v[204:205]
	v_mov_b64_e32 v[130:131], v[206:207]
	v_mov_b64_e32 v[132:133], v[208:209]
	v_mov_b64_e32 v[134:135], v[210:211]
	v_mov_b64_e32 v[136:137], v[212:213]
	v_mov_b64_e32 v[138:139], v[226:227]
	v_mov_b64_e32 v[140:141], v[228:229]
	v_mov_b64_e32 v[142:143], v[230:231]
	v_mov_b64_e32 v[144:145], v[232:233]
	v_pk_mul_f32 v[100:101], v[100:101], v[108:109]
	v_pk_mul_f32 v[104:105], v[104:105], v[112:113]
	v_pk_mul_f32 v[106:107], v[106:107], v[114:115]
	v_pk_add_f32 v[112:113], v[136:137], 1.0 op_sel_hi:[1,0]
	v_pk_add_f32 v[114:115], v[134:135], 1.0 op_sel_hi:[1,0]
	v_pk_mul_f32 v[102:103], v[102:103], v[110:111]
	v_pk_add_f32 v[108:109], v[132:133], 1.0 op_sel_hi:[1,0]
	v_pk_add_f32 v[110:111], v[130:131], 1.0 op_sel_hi:[1,0]
	v_pk_fma_f32 v[106:107], v[112:113], v[106:107], v[144:145]
	v_pk_fma_f32 v[104:105], v[114:115], v[104:105], v[142:143]
	v_pk_fma_f32 v[108:109], v[108:109], v[102:103], v[140:141]
	v_pk_fma_f32 v[102:103], v[110:111], v[100:101], v[138:139]
	v_cvt_pk_bf16_f32 v100, v104, v105
	v_cvt_pk_bf16_f32 v101, v106, v107
	v_cvt_pk_bf16_f32 v102, v102, v103
	v_cvt_pk_bf16_f32 v103, v108, v109
	global_store_dwordx4 v[146:147], v[100:103], off offset:1024
.LBB0_3038:
	s_andn2_b64 vcc, exec, s[12:13]
	s_mov_b64 s[12:13], 0
	s_cbranch_vccnz .LBB0_3035
	s_add_i32 s4, s6, 0x1000
	s_cmp_lt_i32 s4, s36
	s_cselect_b64 s[12:13], -1, 0
	s_and_b64 s[14:15], s[12:13], exec
	s_cselect_b32 s14, s4, s10
	s_ashr_i32 s15, s14, 31
	s_min_i32 s7, s10, 0x4000
	s_lshl_b64 s[16:17], s[14:15], 13
	s_lshl_b64 s[14:15], s[14:15], 12
	s_ashr_i32 s7, s7, 12
	s_waitcnt vmcnt(4)
	v_lshlrev_b32_e32 v100, 16, v94
	v_and_b32_e32 v101, 0xffff0000, v94
	v_lshlrev_b32_e32 v94, 16, v95
	v_and_b32_e32 v95, 0xffff0000, v95
	v_lshl_add_u64 v[46:47], v[120:121], 0, s[14:15]
	s_mul_hi_i32 s15, s7, 0x1800
	s_mul_i32 s14, s7, 0x1800
	v_pk_add_f32 v[94:95], v[94:95], 0 op_sel_hi:[1,0]
	v_lshlrev_b32_e32 v102, 16, v96
	v_and_b32_e32 v103, 0xffff0000, v96
	v_lshlrev_b32_e32 v96, 16, v97
	v_and_b32_e32 v97, 0xffff0000, v97
	v_lshlrev_b32_e32 v104, 16, v90
	v_and_b32_e32 v105, 0xffff0000, v90
	v_lshlrev_b32_e32 v90, 16, v91
	v_and_b32_e32 v91, 0xffff0000, v91
	s_lshl_b64 s[14:15], s[14:15], 2
	v_pk_add_f32 v[100:101], v[100:101], 0 op_sel_hi:[1,0]
	v_pk_add_f32 v[96:97], v[96:97], 0 op_sel_hi:[1,0]
	v_pk_add_f32 v[90:91], v[94:95], v[90:91]
	v_lshlrev_b32_e32 v94, 16, v92
	v_and_b32_e32 v95, 0xffff0000, v92
	v_lshlrev_b32_e32 v92, 16, v93
	v_and_b32_e32 v93, 0xffff0000, v93
	s_add_u32 s7, s37, s14
	v_pk_add_f32 v[102:103], v[102:103], 0 op_sel_hi:[1,0]
	v_pk_add_f32 v[100:101], v[100:101], v[104:105]
	v_pk_add_f32 v[92:93], v[96:97], v[92:93]
	v_lshlrev_b32_e32 v96, 16, v86
	v_and_b32_e32 v97, 0xffff0000, v86
	v_lshlrev_b32_e32 v86, 16, v87
	v_and_b32_e32 v87, 0xffff0000, v87
	v_lshl_add_u64 v[30:31], v[118:119], 0, s[16:17]
	s_addc_u32 s11, s38, s15
	v_pk_add_f32 v[94:95], v[102:103], v[94:95]
	v_pk_add_f32 v[86:87], v[90:91], v[86:87]
	v_pk_add_f32 v[90:91], v[100:101], v[96:97]
	v_lshlrev_b32_e32 v96, 16, v88
	v_and_b32_e32 v97, 0xffff0000, v88
	v_lshlrev_b32_e32 v88, 16, v89
	v_and_b32_e32 v89, 0xffff0000, v89
	v_add_co_u32_e32 v38, vcc, 0x1000, v30
	s_add_u32 s16, s7, 0x5000
	v_pk_add_f32 v[88:89], v[92:93], v[88:89]
	v_pk_add_f32 v[92:93], v[94:95], v[96:97]
	v_lshlrev_b32_e32 v94, 16, v82
	v_and_b32_e32 v95, 0xffff0000, v82
	v_lshlrev_b32_e32 v96, 16, v83
	v_and_b32_e32 v97, 0xffff0000, v83
	v_addc_co_u32_e32 v39, vcc, 0, v31, vcc
	s_addc_u32 s17, s11, 0
	v_pk_add_f32 v[82:83], v[90:91], v[94:95]
	v_pk_add_f32 v[94:95], v[86:87], v[96:97]
	v_lshlrev_b32_e32 v86, 16, v84
	v_and_b32_e32 v87, 0xffff0000, v84
	v_lshlrev_b32_e32 v84, 16, v85
	v_and_b32_e32 v85, 0xffff0000, v85
	v_pk_add_f32 v[92:93], v[92:93], v[86:87]
	v_pk_add_f32 v[96:97], v[88:89], v[84:85]
	global_load_dwordx4 v[84:87], v117, s[16:17] offset:16
	global_load_dwordx4 v[88:91], v117, s[16:17]
	global_load_dwordx4 v[162:165], v123, s[16:17] offset:16
	global_load_dwordx4 v[166:169], v123, s[16:17]
	s_add_u32 s14, s39, s14
	s_addc_u32 s15, s40, s15
	s_add_u32 s16, s14, 0x1000
	s_addc_u32 s17, s15, 0
	global_load_dwordx4 v[174:177], v[124:125], off offset:16
	global_load_dwordx4 v[178:181], v[124:125], off
	global_load_dwordx4 v[182:185], v117, s[16:17] offset:16
	global_load_dwordx4 v[186:189], v117, s[16:17]
	global_load_dwordx4 v[190:193], v117, s[14:15] offset:16
	global_load_dwordx4 v[194:197], v117, s[14:15]
	global_load_dwordx4 v[198:201], v[124:125], off offset:2064
	global_load_dwordx4 v[202:205], v[124:125], off offset:2048
	global_load_dwordx4 v[206:209], v123, s[16:17] offset:16
	global_load_dwordx4 v[210:213], v123, s[16:17]
	global_load_dwordx4 v[226:229], v117, s[14:15] offset:2064
	global_load_dwordx4 v[230:233], v117, s[14:15] offset:2048
	global_load_dwordx4 v[2:5], v[30:31], off nt
	global_load_dwordx4 v[14:17], v[30:31], off offset:2048 nt
	global_load_dwordx4 v[18:21], v[38:39], off nt
	global_load_dwordx4 v[26:29], v[38:39], off offset:2048 nt
	global_load_dwordx4 v[6:9], v[46:47], off offset:16
	global_load_dwordx4 v[10:13], v[46:47], off
	global_load_dwordx4 v[22:25], v[30:31], off offset:1024 nt
	s_nop 0
	global_load_dwordx4 v[30:33], v[30:31], off offset:3072 nt
	s_nop 0
	global_load_dwordx4 v[34:37], v[38:39], off offset:1024 nt
	s_nop 0
	global_load_dwordx4 v[38:41], v[38:39], off offset:3072 nt
	s_nop 0
	global_load_dwordx4 v[42:45], v[46:47], off offset:2064
	s_nop 0
	global_load_dwordx4 v[46:49], v[46:47], off offset:2048
	s_ashr_i32 s11, s10, 31
	s_lshl_b64 s[18:19], s[10:11], 12
	s_and_b64 vcc, exec, s[34:35]
	s_waitcnt vmcnt(27)
	v_pk_fma_f32 v[74:75], v[92:93], v[84:85], v[74:75]
	v_lshlrev_b32_e32 v84, 16, v70
	v_and_b32_e32 v85, 0xffff0000, v70
	v_lshlrev_b32_e32 v70, 16, v71
	v_and_b32_e32 v71, 0xffff0000, v71
	s_waitcnt vmcnt(26)
	v_pk_fma_f32 v[78:79], v[82:83], v[88:89], v[78:79]
	v_pk_fma_f32 v[76:77], v[96:97], v[86:87], v[76:77]
	v_pk_add_f32 v[70:71], v[70:71], 0 op_sel_hi:[1,0]
	v_lshlrev_b32_e32 v86, 16, v72
	v_and_b32_e32 v87, 0xffff0000, v72
	v_lshlrev_b32_e32 v72, 16, v73
	v_and_b32_e32 v73, 0xffff0000, v73
	v_lshlrev_b32_e32 v88, 16, v66
	v_and_b32_e32 v89, 0xffff0000, v66
	v_lshlrev_b32_e32 v66, 16, v67
	v_and_b32_e32 v67, 0xffff0000, v67
	v_pk_add_f32 v[84:85], v[84:85], 0 op_sel_hi:[1,0]
	v_pk_add_f32 v[72:73], v[72:73], 0 op_sel_hi:[1,0]
	v_pk_add_f32 v[66:67], v[70:71], v[66:67]
	v_lshlrev_b32_e32 v70, 16, v68
	v_and_b32_e32 v71, 0xffff0000, v68
	v_lshlrev_b32_e32 v68, 16, v69
	v_and_b32_e32 v69, 0xffff0000, v69
	v_pk_add_f32 v[86:87], v[86:87], 0 op_sel_hi:[1,0]
	v_pk_add_f32 v[84:85], v[84:85], v[88:89]
	v_pk_add_f32 v[68:69], v[72:73], v[68:69]
	v_lshlrev_b32_e32 v72, 16, v62
	v_and_b32_e32 v73, 0xffff0000, v62
	v_lshlrev_b32_e32 v62, 16, v63
	v_and_b32_e32 v63, 0xffff0000, v63
	v_pk_add_f32 v[70:71], v[86:87], v[70:71]
	v_pk_add_f32 v[62:63], v[66:67], v[62:63]
	v_pk_add_f32 v[66:67], v[84:85], v[72:73]
	v_lshlrev_b32_e32 v72, 16, v64
	v_and_b32_e32 v73, 0xffff0000, v64
	v_lshlrev_b32_e32 v64, 16, v65
	v_and_b32_e32 v65, 0xffff0000, v65
	v_pk_fma_f32 v[80:81], v[94:95], v[90:91], v[80:81]
	v_lshl_add_u64 v[82:83], v[126:127], 0, s[18:19]
	v_pk_add_f32 v[64:65], v[68:69], v[64:65]
	v_pk_add_f32 v[68:69], v[70:71], v[72:73]
	v_lshlrev_b32_e32 v70, 16, v58
	v_and_b32_e32 v71, 0xffff0000, v58
	v_lshlrev_b32_e32 v58, 16, v59
	v_and_b32_e32 v59, 0xffff0000, v59
	global_store_dwordx4 v[82:83], v[78:81], off
	global_store_dwordx4 v[82:83], v[74:77], off offset:16
	v_pk_add_f32 v[66:67], v[66:67], v[70:71]
	v_pk_add_f32 v[70:71], v[62:63], v[58:59]
	v_lshlrev_b32_e32 v58, 16, v60
	v_and_b32_e32 v59, 0xffff0000, v60
	v_lshlrev_b32_e32 v60, 16, v61
	v_and_b32_e32 v61, 0xffff0000, v61
	v_pk_add_f32 v[68:69], v[68:69], v[58:59]
	v_pk_add_f32 v[72:73], v[64:65], v[60:61]
	s_waitcnt vmcnt(26)
	v_pk_fma_f32 v[52:53], v[72:73], v[164:165], v[52:53]
	v_pk_fma_f32 v[56:57], v[70:71], v[168:169], v[56:57]
	v_pk_fma_f32 v[54:55], v[66:67], v[166:167], v[54:55]
	v_pk_fma_f32 v[50:51], v[68:69], v[162:163], v[50:51]
	global_store_dwordx4 v[82:83], v[54:57], off offset:2048
	global_store_dwordx4 v[82:83], v[50:53], off offset:2064
	s_cbranch_vccnz .LBB0_3034
	v_pk_mul_f32 v[58:59], v[80:81], v[80:81]
	v_pk_mul_f32 v[60:61], v[78:79], v[78:79]
	v_pk_mov_b32 v[62:63], v[60:61], v[58:59] op_sel:[1,0]
	v_mov_b32_e32 v61, v59
	v_pk_add_f32 v[58:59], v[62:63], v[60:61]
	v_pk_mul_f32 v[60:61], v[76:77], v[76:77]
	v_pk_mul_f32 v[62:63], v[74:75], v[74:75]
	v_pk_add_f32 v[58:59], v[58:59], v[58:59] op_sel:[0,1] op_sel_hi:[1,0]
	v_pk_mov_b32 v[64:65], v[62:63], v[60:61] op_sel:[1,0]
	v_mov_b32_e32 v63, v61
	v_pk_add_f32 v[60:61], v[64:65], v[62:63]
	v_mul_f32_e32 v62, v50, v50
	v_mul_f32_e32 v63, v51, v51
	v_pk_add_f32 v[60:61], v[60:61], v[60:61] op_sel:[0,1] op_sel_hi:[1,0]
	v_mov_b32_e32 v59, v62
	v_mov_b32_e32 v61, v63
	v_pk_add_f32 v[58:59], v[58:59], v[60:61]
	v_mul_f32_e32 v60, v55, v55
	v_mul_f32_e32 v62, v57, v57
	v_mul_f32_e32 v64, v52, v52
	v_mul_f32_e32 v65, v53, v53
	v_pk_fma_f32 v[60:61], v[54:55], v[54:55], v[60:61] op_sel_hi:[1,1,0]
	v_pk_fma_f32 v[62:63], v[56:57], v[56:57], v[62:63] op_sel_hi:[1,1,0]
	v_mov_b32_e32 v61, v64
	v_mov_b32_e32 v63, v65
	v_pk_add_f32 v[60:61], v[60:61], v[62:63]
	v_pk_add_f32 v[58:59], v[58:59], v[60:61]
	v_and_b32_e32 v60, 64, v214
	v_add_f32_e32 v58, v58, v59
	v_xor_b32_e32 v59, 16, v214
	v_add_u32_e32 v60, 64, v60
	v_add_f32_dpp v58, v58, v58 quad_perm:[1,0,3,2] row_mask:0xf bank_mask:0xf bound_ctrl:1
	v_cmp_lt_i32_e32 vcc, v59, v60
	v_add_f32_dpp v58, v58, v58 quad_perm:[2,3,0,1] row_mask:0xf bank_mask:0xf bound_ctrl:1
	v_cndmask_b32_e32 v59, v214, v59, vcc
	v_lshlrev_b32_e32 v59, 2, v59
	v_add_f32_dpp v58, v58, v58 row_half_mirror row_mask:0xf bank_mask:0xf bound_ctrl:1
	s_lshl_b64 s[10:11], s[10:11], 11
	v_add_f32_dpp v58, v58, v58 row_mirror row_mask:0xf bank_mask:0xf bound_ctrl:1
	ds_bpermute_b32 v59, v59, v58
	s_waitcnt lgkmcnt(0)
	v_add_f32_e32 v58, v58, v59
	v_xor_b32_e32 v59, 32, v214
	v_cmp_lt_i32_e32 vcc, v59, v60
	s_nop 1
	v_cndmask_b32_e32 v59, v214, v59, vcc
	v_lshlrev_b32_e32 v59, 2, v59
	ds_bpermute_b32 v59, v59, v58
	s_waitcnt lgkmcnt(0)
	v_add_f32_e32 v58, v58, v59
	v_fmamk_f32 v58, v58, 0x3a800000, v1
	v_cmp_gt_f32_e32 vcc, s77, v58
	v_mul_f32_e32 v59, 0x4b800000, v58
	s_nop 0
	v_cndmask_b32_e32 v58, v58, v59, vcc
	v_rsq_f32_e32 v58, v58
	s_nop 0
	v_mul_f32_e32 v59, 0x45800000, v58
	v_cndmask_b32_e32 v62, v58, v59, vcc
	s_waitcnt vmcnt(22)
	v_mov_b64_e32 v[58:59], v[174:175]
	v_mov_b64_e32 v[60:61], v[176:177]
	v_mov_b64_e32 v[64:65], v[178:179]
	v_mov_b64_e32 v[66:67], v[180:181]
	v_mov_b64_e32 v[68:69], v[182:183]
	v_mov_b64_e32 v[70:71], v[184:185]
	v_mov_b64_e32 v[82:83], v[186:187]
	v_mov_b64_e32 v[84:85], v[188:189]
	v_mov_b64_e32 v[86:87], v[190:191]
	v_mov_b64_e32 v[88:89], v[192:193]
	v_mov_b64_e32 v[90:91], v[194:195]
	v_mov_b64_e32 v[92:93], v[196:197]
	v_pk_mul_f32 v[72:73], v[80:81], v[62:63] op_sel_hi:[1,0]
	v_pk_mul_f32 v[78:79], v[78:79], v[62:63] op_sel_hi:[1,0]
	v_pk_mul_f32 v[74:75], v[74:75], v[62:63] op_sel_hi:[1,0]
	v_pk_mul_f32 v[56:57], v[56:57], v[62:63] op_sel_hi:[1,0]
	v_pk_mul_f32 v[54:55], v[54:55], v[62:63] op_sel_hi:[1,0]
	v_pk_mul_f32 v[52:53], v[52:53], v[62:63] op_sel_hi:[1,0]
	v_pk_mul_f32 v[50:51], v[50:51], v[62:63] op_sel_hi:[1,0]
	v_pk_mul_f32 v[58:59], v[58:59], v[74:75]
	v_pk_mul_f32 v[66:67], v[66:67], v[72:73]
	v_pk_mul_f32 v[64:65], v[64:65], v[78:79]
	v_pk_add_f32 v[72:73], v[84:85], 1.0 op_sel_hi:[1,0]
	v_pk_add_f32 v[78:79], v[82:83], 1.0 op_sel_hi:[1,0]
	v_pk_fma_f32 v[66:67], v[72:73], v[66:67], v[92:93]
	v_pk_mul_f32 v[72:73], v[76:77], v[62:63] op_sel_hi:[1,0]
	v_pk_add_f32 v[70:71], v[70:71], 1.0 op_sel_hi:[1,0]
	v_pk_mul_f32 v[60:61], v[60:61], v[72:73]
	v_pk_add_f32 v[68:69], v[68:69], 1.0 op_sel_hi:[1,0]
	v_pk_fma_f32 v[64:65], v[78:79], v[64:65], v[90:91]
	v_pk_fma_f32 v[70:71], v[70:71], v[60:61], v[88:89]
	v_pk_fma_f32 v[60:61], v[68:69], v[58:59], v[86:87]
	v_cvt_pk_bf16_f32 v58, v64, v65
	v_cvt_pk_bf16_f32 v59, v66, v67
	v_cvt_pk_bf16_f32 v60, v60, v61
	v_cvt_pk_bf16_f32 v61, v70, v71
	v_lshl_add_u64 v[84:85], v[128:129], 0, s[10:11]
	global_store_dwordx4 v[84:85], v[58:61], off
	s_waitcnt vmcnt(17)
	s_nop 1
	v_mov_b64_e32 v[58:59], v[198:199]
	v_mov_b64_e32 v[60:61], v[200:201]
	s_nop 0
	v_mov_b64_e32 v[64:65], v[202:203]
	v_mov_b64_e32 v[66:67], v[204:205]
	v_mov_b64_e32 v[68:69], v[206:207]
	v_mov_b64_e32 v[70:71], v[208:209]
	v_mov_b64_e32 v[72:73], v[210:211]
	v_mov_b64_e32 v[74:75], v[212:213]
	v_mov_b64_e32 v[76:77], v[226:227]
	v_mov_b64_e32 v[78:79], v[228:229]
	v_mov_b64_e32 v[80:81], v[230:231]
	v_mov_b64_e32 v[82:83], v[232:233]
	v_pk_mul_f32 v[50:51], v[58:59], v[50:51]
	v_pk_mul_f32 v[54:55], v[64:65], v[54:55]
	v_pk_mul_f32 v[56:57], v[66:67], v[56:57]
	v_pk_add_f32 v[64:65], v[74:75], 1.0 op_sel_hi:[1,0]
	v_pk_add_f32 v[66:67], v[72:73], 1.0 op_sel_hi:[1,0]
	v_pk_mul_f32 v[52:53], v[60:61], v[52:53]
	v_pk_add_f32 v[58:59], v[70:71], 1.0 op_sel_hi:[1,0]
	v_pk_add_f32 v[60:61], v[68:69], 1.0 op_sel_hi:[1,0]
	v_pk_fma_f32 v[56:57], v[64:65], v[56:57], v[82:83]
	v_pk_fma_f32 v[54:55], v[66:67], v[54:55], v[80:81]
	v_pk_fma_f32 v[58:59], v[58:59], v[52:53], v[78:79]
	v_pk_fma_f32 v[52:53], v[60:61], v[50:51], v[76:77]
	v_cvt_pk_bf16_f32 v50, v54, v55
	v_cvt_pk_bf16_f32 v51, v56, v57
	v_cvt_pk_bf16_f32 v52, v52, v53
	v_cvt_pk_bf16_f32 v53, v58, v59
	global_store_dwordx4 v[84:85], v[50:53], off offset:1024
	s_branch .LBB0_3034
